# baseline (speedup 1.0000x reference)
_Z5k_aggPKDF16_PKhPKiS4_PKDv8_DF16_PKfPDF16_Pf:
	s_load_dwordx8 s[4:11], s[0:1], 0x8
	s_load_dwordx4 s[12:15], s[0:1], 0x28
	s_load_dwordx2 s[16:17], s[0:1], 0x38
	v_lshlrev_b32_e32 v2, 4, v0
	s_lshl_b32 s0, s2, 2
	s_lshl_b32 s1, s2, 3
	s_andn2_b32 s0, s0, 63
	s_and_b32 s1, s1, 56
	s_or_b32 s0, s0, s1
	s_lshr_b32 s1, s2, 1
	s_and_b32 s1, s1, 4
	s_or_b32 s0, s0, s1
	v_lshlrev_b32_e32 v1, 2, v0
	v_lshrrev_b32_e32 v52, 6, v0
	v_or_b32_e32 v3, s0, v52
	v_mov_b32_e32 v98, v2
	s_waitcnt lgkmcnt(0)
	v_readfirstlane_b32 s19, v52
	s_nop 3
	s_lshl_b32 s19, s19, 10
	s_mov_b32 m0, s19
	s_nop 0
	global_load_lds_dwordx4 v2, s[10:11]
	s_add_u32 m0, s19, 0x1000
	v_add_u32_e32 v96, 0x1000, v2
	global_load_lds_dwordx4 v96, s[10:11]
	s_add_u32 m0, s19, 0x2000
	v_add_u32_e32 v96, 0x2000, v2
	global_load_lds_dwordx4 v96, s[10:11]
	s_add_u32 m0, s19, 0x3000
	v_add_u32_e32 v96, 0x3000, v2
	global_load_lds_dwordx4 v96, s[10:11]
	s_add_u32 m0, s19, 0x4000
	v_add_u32_e32 v96, 0x4000, v2
	global_load_lds_dwordx4 v96, s[10:11]
	s_add_u32 m0, s19, 0x5000
	v_add_u32_e32 v96, 0x5000, v2
	global_load_lds_dwordx4 v96, s[10:11]
	s_add_u32 m0, s19, 0x6000
	v_add_u32_e32 v96, 0x6000, v2
	global_load_lds_dwordx4 v96, s[10:11]
	s_add_u32 m0, s19, 0x7000
	v_add_u32_e32 v96, 0x7000, v2
	global_load_lds_dwordx4 v96, s[10:11]
	v_mov_b32_e32 v97, 0
	ds_write2st64_b32 v1, v97, v97 offset0:128 offset1:132
	ds_write2st64_b32 v1, v97, v97 offset0:136 offset1:140
	s_movk_i32 s0, 0x186a
	v_cmp_gt_i32_e32 vcc, s0, v3
	s_and_saveexec_b64 s[0:1], vcc
	s_cbranch_execz .Lagg_invalid
	v_bfe_u32 v4, v0, 2, 4
	v_lshlrev_b32_e32 v53, 4, v3
	v_or_b32_e32 v10, v53, v4
	v_and_b32_e32 v54, 48, v2
	v_lshl_or_b32 v11, v10, 7, v54
	global_load_dwordx4 v[2:5], v11, s[4:5]
	global_load_dwordx4 v[6:9], v11, s[4:5] offset:64
	v_ashrrev_i32_e32 v11, 31, v10
	v_lshl_add_u64 v[10:11], v[10:11], 2, s[6:7]
	global_load_dwordx2 v[50:51], v[10:11], off
	s_waitcnt vmcnt(2)
	v_cvt_pk_f32_fp8_e32 v[10:11], v2
	v_cvt_pk_f32_fp8_sdwa v[12:13], v2 src0_sel:WORD_1
	v_cvt_pk_f32_fp8_e32 v[14:15], v3
	v_cvt_pk_f32_fp8_sdwa v[2:3], v3 src0_sel:WORD_1
	v_cvt_pk_f32_fp8_e32 v[16:17], v4
	v_cvt_pk_f32_fp8_sdwa v[18:19], v4 src0_sel:WORD_1
	v_cvt_pk_f32_fp8_e32 v[20:21], v5
	v_cvt_pk_f32_fp8_sdwa v[4:5], v5 src0_sel:WORD_1
	s_waitcnt vmcnt(1)
	v_cvt_pk_f32_fp8_e32 v[22:23], v6
	v_cvt_pk_f32_fp8_sdwa v[24:25], v6 src0_sel:WORD_1
	v_cvt_pk_f32_fp8_e32 v[26:27], v7
	v_cvt_pk_f32_fp8_sdwa v[6:7], v7 src0_sel:WORD_1
	v_cvt_pk_f32_fp8_e32 v[28:29], v8
	v_cvt_pk_f32_fp8_sdwa v[30:31], v8 src0_sel:WORD_1
	v_cvt_pk_f32_fp8_e32 v[32:33], v9
	v_cvt_pk_f32_fp8_sdwa v[8:9], v9 src0_sel:WORD_1
	v_add_f32_e32 v88, 0, v10
	v_add_f32_e32 v89, 0, v11
	v_add_f32_e32 v90, 0, v12
	v_add_f32_e32 v91, 0, v13
	v_add_f32_e32 v92, 0, v14
	v_add_f32_e32 v93, 0, v15
	v_add_f32_e32 v94, 0, v2
	v_add_f32_e32 v95, 0, v3
	v_add_f32_e32 v76, 0, v16
	v_add_f32_e32 v77, 0, v17
	v_add_f32_e32 v80, 0, v18
	v_add_f32_e32 v81, 0, v19
	v_add_f32_e32 v84, 0, v20
	v_add_f32_e32 v85, 0, v21
	v_add_f32_e32 v86, 0, v4
	v_add_f32_e32 v87, 0, v5
	v_add_f32_e32 v72, 0, v22
	v_add_f32_e32 v73, 0, v23
	v_add_f32_e32 v74, 0, v24
	v_add_f32_e32 v75, 0, v25
	v_add_f32_e32 v78, 0, v26
	v_add_f32_e32 v79, 0, v27
	v_add_f32_e32 v82, 0, v6
	v_add_f32_e32 v83, 0, v7
	v_add_f32_e32 v64, 0, v28
	v_add_f32_e32 v65, 0, v29
	v_add_f32_e32 v66, 0, v30
	v_add_f32_e32 v67, 0, v31
	v_add_f32_e32 v68, 0, v32
	v_add_f32_e32 v69, 0, v33
	v_add_f32_e32 v70, 0, v8
	v_add_f32_e32 v71, 0, v9
	s_waitcnt vmcnt(0)
	s_mov_b64 s[6:7], exec
	v_mov_b32_e32 v63, 0xc35000
	v_add_u32_e32 v106, 0, v50
	v_lshlrev_b32_e32 v106, 2, v106
	global_load_dwordx3 v[56:58], v106, s[8:9]
	v_add_u32_e32 v106, 3, v50
	v_lshlrev_b32_e32 v106, 2, v106
	global_load_dwordx3 v[60:62], v106, s[8:9]
	s_waitcnt vmcnt(0)
	v_add_u32_e32 v104, 0, v50
	v_cmp_lt_i32_e32 vcc, v104, v51
	v_lshlrev_b32_e32 v105, 7, v56
	s_nop 0
	v_cndmask_b32_e32 v105, v63, v105, vcc
	v_or_b32_e32 v105, v54, v105
	global_load_dwordx4 v[2:5], v105, s[4:5]
	global_load_dwordx4 v[6:9], v105, s[4:5] offset:64
	v_add_u32_e32 v104, 1, v50
	v_cmp_lt_i32_e32 vcc, v104, v51
	v_lshlrev_b32_e32 v105, 7, v57
	s_nop 0
	v_cndmask_b32_e32 v105, v63, v105, vcc
	v_or_b32_e32 v105, v54, v105
	global_load_dwordx4 v[10:13], v105, s[4:5]
	global_load_dwordx4 v[14:17], v105, s[4:5] offset:64
	v_add_u32_e32 v104, 2, v50
	v_cmp_lt_i32_e32 vcc, v104, v51
	v_lshlrev_b32_e32 v105, 7, v58
	s_nop 0
	v_cndmask_b32_e32 v105, v63, v105, vcc
	v_or_b32_e32 v105, v54, v105
	global_load_dwordx4 v[18:21], v105, s[4:5]
	global_load_dwordx4 v[22:25], v105, s[4:5] offset:64
	v_add_u32_e32 v106, 6, v50
	v_lshlrev_b32_e32 v106, 2, v106
	global_load_dwordx3 v[56:58], v106, s[8:9]
	v_add_u32_e32 v104, 3, v50
	v_cmp_lt_i32_e32 vcc, v104, v51
	v_lshlrev_b32_e32 v105, 7, v60
	s_nop 0
	v_cndmask_b32_e32 v105, v63, v105, vcc
	v_or_b32_e32 v105, v54, v105
	global_load_dwordx4 v[26:29], v105, s[4:5]
	global_load_dwordx4 v[30:33], v105, s[4:5] offset:64
	v_add_u32_e32 v104, 4, v50
	v_cmp_lt_i32_e32 vcc, v104, v51
	v_lshlrev_b32_e32 v105, 7, v61
	s_nop 0
	v_cndmask_b32_e32 v105, v63, v105, vcc
	v_or_b32_e32 v105, v54, v105
	global_load_dwordx4 v[34:37], v105, s[4:5]
	global_load_dwordx4 v[38:41], v105, s[4:5] offset:64
	v_add_u32_e32 v104, 5, v50
	v_cmp_lt_i32_e32 vcc, v104, v51
	v_lshlrev_b32_e32 v105, 7, v62
	s_nop 0
	v_cndmask_b32_e32 v105, v63, v105, vcc
	v_or_b32_e32 v105, v54, v105
	global_load_dwordx4 v[42:45], v105, s[4:5]
	global_load_dwordx4 v[46:49], v105, s[4:5] offset:64
	v_add_u32_e32 v106, 9, v50
	v_lshlrev_b32_e32 v106, 2, v106
	global_load_dwordx3 v[60:62], v106, s[8:9]
	.p2align	6
